# speedup vs baseline: 1.0151x; 1.0039x over previous
.LBB4_4:
	s_load_dword s2, s[0:1], 0x18
	v_lshrrev_b32_e32 v6, 4, v0
	v_xor_b32_e32 v1, v6, v0
	v_lshlrev_b32_e32 v1, 3, v1
	v_and_b32_e32 v2, 56, v1
	v_lshrrev_b32_e32 v1, 3, v0
	s_waitcnt lgkmcnt(0)
	v_mad_u64_u32 v[4:5], s[0:1], v1, s2, v[2:3]
	v_or_b32_e32 v3, 0x200, v0
	v_lshrrev_b32_e32 v3, 3, v3
	s_lshl_b32 s10, s12, 7
	s_ashr_i32 s13, s2, 31
	v_mul_lo_u32 v3, v3, s2
	s_lshl_b32 s0, s2, 7
	v_add_lshl_u32 v2, v3, v2, 1
	v_add_lshl_u32 v3, v4, s0, 1
	s_mul_i32 s0, s10, s13
	s_mul_hi_u32 s1, s10, s2
	s_add_i32 s1, s1, s0
	s_mul_i32 s0, s10, s2
	s_mul_i32 s11, s3, 0xc0
	s_lshl_b64 s[0:1], s[0:1], 1
	v_lshlrev_b32_e32 v122, 4, v0
	v_lshlrev_b32_e32 v1, 1, v4
	s_add_u32 s0, s4, s0
	s_mul_i32 s3, s11, s13
	s_mul_hi_u32 s4, s11, s2
	v_add_u32_e32 v4, 0, v122
	s_addc_u32 s1, s5, s1
	s_add_i32 s3, s4, s3
	s_mul_i32 s2, s11, s2
	v_readfirstlane_b32 s13, v4
	v_add_u32_e32 v5, 0x2000, v4
	s_lshl_b64 s[2:3], s[2:3], 1
	s_mov_b32 m0, s13
	v_readfirstlane_b32 s4, v5
	v_add_u32_e32 v5, 0x4000, v4
	s_add_u32 s2, s6, s2
	global_load_lds_dwordx4 v1, s[0:1]
	s_mov_b32 m0, s4
	v_readfirstlane_b32 s5, v5
	v_add_u32_e32 v5, 0x6000, v4
	s_addc_u32 s3, s7, s3
	global_load_lds_dwordx4 v2, s[0:1]
	s_mov_b32 m0, s5
	v_readfirstlane_b32 s6, v5
	v_add_u32_e32 v5, 0x8000, v4
	global_load_lds_dwordx4 v1, s[2:3]
	s_mov_b32 m0, s6
	v_readfirstlane_b32 s7, v5
	v_add_u32_e32 v5, 0xa000, v4
	global_load_lds_dwordx4 v2, s[2:3]
	s_mov_b32 m0, s7
	s_add_u32 s16, s0, 0x80
	v_readfirstlane_b32 s18, v5
	v_add_u32_e32 v5, 0xc000, v4
	global_load_lds_dwordx4 v3, s[2:3]
	s_addc_u32 s17, s1, 0
	s_mov_b32 m0, s18
	v_readfirstlane_b32 s14, v5
	v_add_u32_e32 v5, 0xe000, v4
	s_add_u32 s20, s2, 0x80
	global_load_lds_dwordx4 v1, s[16:17]
	s_mov_b32 m0, s14
	v_readfirstlane_b32 s15, v5
	v_add_u32_e32 v5, 0x10000, v4
	s_addc_u32 s21, s3, 0
	global_load_lds_dwordx4 v2, s[16:17]
	s_mov_b32 m0, s15
	v_readfirstlane_b32 s16, v5
	v_add_u32_e32 v5, 0x12000, v4
	global_load_lds_dwordx4 v1, s[20:21]
	s_mov_b32 m0, s16
	v_readfirstlane_b32 s17, v5
	global_load_lds_dwordx4 v2, s[20:21]
	s_mov_b32 m0, s17
	v_add_u32_e32 v5, 0x14000, v4
	global_load_lds_dwordx4 v3, s[20:21]
	s_add_u32 s20, s0, 0x100
	v_readfirstlane_b32 s19, v5
	v_add_u32_e32 v5, 0x16000, v4
	s_addc_u32 s21, s1, 0
	s_mov_b32 m0, s19
	v_readfirstlane_b32 s19, v5
	v_add_u32_e32 v5, 0x18000, v4
	s_add_u32 s22, s2, 0x100
	global_load_lds_dwordx4 v1, s[20:21]
	s_mov_b32 m0, s19
	v_readfirstlane_b32 s19, v5
	v_add_u32_e32 v5, 0x1a000, v4
	s_addc_u32 s23, s3, 0
	global_load_lds_dwordx4 v2, s[20:21]
	s_mov_b32 m0, s19
	v_readfirstlane_b32 s19, v5
	v_add_u32_e32 v4, 0x1c000, v4
	global_load_lds_dwordx4 v1, s[22:23]
	s_mov_b32 m0, s19
	v_readfirstlane_b32 s19, v4
	global_load_lds_dwordx4 v2, s[22:23]
	s_mov_b32 m0, s19
	v_and_b32_e32 v8, 15, v0
	global_load_lds_dwordx4 v3, s[22:23]
	v_lshrrev_b32_e32 v11, 2, v0
	v_bfe_u32 v9, v0, 6, 2
	v_bfe_u32 v5, v0, 1, 3
	v_and_or_b32 v4, v11, 64, v8
	v_lshlrev_b32_e32 v123, 7, v4
	v_bitop3_b32 v4, v6, v5, 3 bitop3:0x6c
	v_mul_u32_u24_e32 v10, 48, v9
	v_lshlrev_b32_e32 v6, 4, v4
	v_or_b32_e32 v4, v10, v8
	v_lshlrev_b32_e32 v7, 7, v4
	v_add_u32_e32 v13, 0, v7
	s_waitcnt vmcnt(10)
	s_barrier
	v_add_u32_e32 v4, v13, v6
	ds_read_b128 v[14:17], v4 offset:16384
	v_add_u32_e32 v50, 0, v123
	v_add_u32_e32 v6, v50, v6
	ds_read_b128 v[18:21], v6
	ds_read_b128 v[22:25], v4 offset:18432
	ds_read_b128 v[26:29], v6 offset:2048
	ds_read_b128 v[30:33], v4 offset:20480
	ds_read_b128 v[42:45], v6 offset:4096
	ds_read_b128 v[46:49], v6 offset:6144
	v_bfe_u32 v12, v0, 4, 2
	v_bitop3_b32 v0, v12, v5, 4 bitop3:0x36
	v_lshlrev_b32_e32 v5, 4, v0
	s_add_i32 s19, 0, 0x14000
	v_add_u32_e32 v124, s19, v5
	s_waitcnt lgkmcnt(0)
	v_mfma_f32_16x16x32_f16 v[34:37], v[14:17], v[18:21], 0
	v_add_u32_e32 v7, v7, v124
	v_mfma_f32_16x16x32_f16 v[38:41], v[22:25], v[18:21], 0
	v_mfma_f32_16x16x32_f16 v[18:21], v[30:33], v[18:21], 0
	v_add_u32_e32 v0, v50, v5
	ds_read_b128 v[50:53], v0
	ds_read_b128 v[54:57], v0 offset:2048
	ds_read_b128 v[58:61], v0 offset:4096
	ds_read_b128 v[62:65], v0 offset:6144
	v_add_u32_e32 v5, v13, v5
	ds_read_b128 v[66:69], v5 offset:16384
	ds_read_b128 v[70:73], v5 offset:18432
	ds_read_b128 v[74:77], v5 offset:20480
	v_mfma_f32_16x16x32_f16 v[78:81], v[14:17], v[26:29], 0
	v_mfma_f32_16x16x32_f16 v[82:85], v[22:25], v[26:29], 0
	v_mfma_f32_16x16x32_f16 v[26:29], v[30:33], v[26:29], 0
	v_mfma_f32_16x16x32_f16 v[86:89], v[14:17], v[42:45], 0
	v_mfma_f32_16x16x32_f16 v[90:93], v[22:25], v[42:45], 0
	v_mfma_f32_16x16x32_f16 v[42:45], v[30:33], v[42:45], 0
	v_mfma_f32_16x16x32_f16 v[14:17], v[14:17], v[46:49], 0
	v_mfma_f32_16x16x32_f16 v[22:25], v[22:25], v[46:49], 0
	v_mfma_f32_16x16x32_f16 v[30:33], v[30:33], v[46:49], 0
	s_add_u32 s20, s0, 0x180
	s_mov_b32 m0, s13
	s_waitcnt vmcnt(5) lgkmcnt(0)
	s_barrier
	s_addc_u32 s21, s1, 0
	s_add_u32 s22, s2, 0x180
	global_load_lds_dwordx4 v1, s[20:21]
	s_mov_b32 m0, s4
	s_addc_u32 s23, s3, 0
	global_load_lds_dwordx4 v2, s[20:21]
	s_mov_b32 m0, s5
	s_nop 0
	global_load_lds_dwordx4 v1, s[22:23]
	s_mov_b32 m0, s6
	s_nop 0
	global_load_lds_dwordx4 v2, s[22:23]
	s_mov_b32 m0, s7
	s_nop 0
	global_load_lds_dwordx4 v3, s[22:23]
	s_waitcnt lgkmcnt(0)
	v_mfma_f32_16x16x32_f16 v[34:37], v[66:69], v[50:53], v[34:37]
	v_mfma_f32_16x16x32_f16 v[38:41], v[70:73], v[50:53], v[38:41]
	v_mfma_f32_16x16x32_f16 v[18:21], v[74:77], v[50:53], v[18:21]
	ds_read_b128 v[46:49], v6 offset:40960
	ds_read_b128 v[50:53], v6 offset:43008
	ds_read_b128 v[94:97], v6 offset:45056
	ds_read_b128 v[98:101], v6 offset:47104
	ds_read_b128 v[102:105], v4 offset:57344
	ds_read_b128 v[106:109], v4 offset:59392
	ds_read_b128 v[110:113], v4 offset:61440
	v_mfma_f32_16x16x32_f16 v[78:81], v[66:69], v[54:57], v[78:81]
	v_mfma_f32_16x16x32_f16 v[82:85], v[70:73], v[54:57], v[82:85]
	v_mfma_f32_16x16x32_f16 v[26:29], v[74:77], v[54:57], v[26:29]
	v_mfma_f32_16x16x32_f16 v[54:57], v[66:69], v[58:61], v[86:89]
	v_mfma_f32_16x16x32_f16 v[86:89], v[70:73], v[58:61], v[90:93]
	v_mfma_f32_16x16x32_f16 v[42:45], v[74:77], v[58:61], v[42:45]
	v_mfma_f32_16x16x32_f16 v[14:17], v[66:69], v[62:65], v[14:17]
	v_mfma_f32_16x16x32_f16 v[22:25], v[70:73], v[62:65], v[22:25]
	v_mfma_f32_16x16x32_f16 v[30:33], v[74:77], v[62:65], v[30:33]
	s_waitcnt lgkmcnt(0)
	v_mfma_f32_16x16x32_f16 v[34:37], v[102:105], v[46:49], v[34:37]
	v_mfma_f32_16x16x32_f16 v[38:41], v[106:109], v[46:49], v[38:41]
	v_mfma_f32_16x16x32_f16 v[18:21], v[110:113], v[46:49], v[18:21]
	ds_read_b128 v[46:49], v0 offset:40960
	ds_read_b128 v[58:61], v0 offset:43008
	ds_read_b128 v[62:65], v0 offset:45056
	ds_read_b128 v[66:69], v0 offset:47104
	ds_read_b128 v[70:73], v5 offset:57344
	ds_read_b128 v[74:77], v5 offset:59392
	ds_read_b128 v[90:93], v5 offset:61440
	v_mfma_f32_16x16x32_f16 v[78:81], v[102:105], v[50:53], v[78:81]
	v_mfma_f32_16x16x32_f16 v[82:85], v[106:109], v[50:53], v[82:85]
	v_mfma_f32_16x16x32_f16 v[26:29], v[110:113], v[50:53], v[26:29]
	v_mfma_f32_16x16x32_f16 v[50:53], v[102:105], v[94:97], v[54:57]
	v_mfma_f32_16x16x32_f16 v[54:57], v[106:109], v[94:97], v[86:89]
	v_mfma_f32_16x16x32_f16 v[42:45], v[110:113], v[94:97], v[42:45]
	v_mfma_f32_16x16x32_f16 v[86:89], v[102:105], v[98:101], v[14:17]
	v_mfma_f32_16x16x32_f16 v[22:25], v[106:109], v[98:101], v[22:25]
	v_mfma_f32_16x16x32_f16 v[30:33], v[110:113], v[98:101], v[30:33]
	s_add_u32 s20, s0, 0x200
	s_mov_b32 m0, s18
	s_waitcnt vmcnt(5) lgkmcnt(0)
	s_barrier
	s_addc_u32 s21, s1, 0
	s_add_u32 s22, s2, 0x200
	global_load_lds_dwordx4 v1, s[20:21]
	s_mov_b32 m0, s14
	s_addc_u32 s23, s3, 0
	global_load_lds_dwordx4 v2, s[20:21]
	s_mov_b32 m0, s15
	s_nop 0
	global_load_lds_dwordx4 v1, s[22:23]
	s_mov_b32 m0, s16
	s_nop 0
	global_load_lds_dwordx4 v2, s[22:23]
	s_mov_b32 m0, s17
	s_nop 0
	global_load_lds_dwordx4 v3, s[22:23]
	s_waitcnt lgkmcnt(0)
	v_mfma_f32_16x16x32_f16 v[34:37], v[70:73], v[46:49], v[34:37]
	v_mfma_f32_16x16x32_f16 v[38:41], v[74:77], v[46:49], v[38:41]
	v_mfma_f32_16x16x32_f16 v[46:49], v[90:93], v[46:49], v[18:21]
	v_add_u32_e32 v13, 0x14000, v6
	v_add_u32_e32 v15, 0x15000, v6
	s_nop 0
	v_add_u32_e32 v18, 0x18000, v4
	v_add_u32_e32 v14, 0x14800, v6
	ds_read_b128 v[94:97], v13
	ds_read_b128 v[98:101], v14
	v_add_u32_e32 v16, 0x15800, v6
	ds_read_b128 v[102:105], v15
	ds_read_b128 v[106:109], v16
	v_add_u32_e32 v19, 0x18800, v4
	ds_read_b128 v[110:113], v18
	ds_read_b128 v[114:117], v19
	v_add_u32_e32 v20, 0x19000, v4
	ds_read_b128 v[118:121], v20
	v_mfma_f32_16x16x32_f16 v[78:81], v[70:73], v[58:61], v[78:81]
	v_mfma_f32_16x16x32_f16 v[82:85], v[74:77], v[58:61], v[82:85]
	v_mfma_f32_16x16x32_f16 v[26:29], v[90:93], v[58:61], v[26:29]
	v_mfma_f32_16x16x32_f16 v[50:53], v[70:73], v[62:65], v[50:53]
	v_mfma_f32_16x16x32_f16 v[54:57], v[74:77], v[62:65], v[54:57]
	v_mfma_f32_16x16x32_f16 v[42:45], v[90:93], v[62:65], v[42:45]
	v_mfma_f32_16x16x32_f16 v[58:61], v[70:73], v[66:69], v[86:89]
	v_mfma_f32_16x16x32_f16 v[22:25], v[74:77], v[66:69], v[22:25]
	v_mfma_f32_16x16x32_f16 v[30:33], v[90:93], v[66:69], v[30:33]
	s_waitcnt lgkmcnt(0)
	v_mfma_f32_16x16x32_f16 v[34:37], v[110:113], v[94:97], v[34:37]
	v_mfma_f32_16x16x32_f16 v[38:41], v[114:117], v[94:97], v[38:41]
	v_mfma_f32_16x16x32_f16 v[46:49], v[118:121], v[94:97], v[46:49]
	v_add_u32_e32 v17, v124, v123
	ds_read_b128 v[62:65], v17 offset:2048
	ds_read_b128 v[66:69], v17 offset:4096
	ds_read_b128 v[70:73], v17 offset:6144
	ds_read_b128 v[74:77], v7 offset:16384
	ds_read_b128 v[86:89], v7 offset:18432
	ds_read_b128 v[90:93], v17
	ds_read_b128 v[94:97], v7 offset:20480
	v_mfma_f32_16x16x32_f16 v[78:81], v[110:113], v[98:101], v[78:81]
	v_mfma_f32_16x16x32_f16 v[82:85], v[114:117], v[98:101], v[82:85]
	v_mfma_f32_16x16x32_f16 v[26:29], v[118:121], v[98:101], v[26:29]
	v_mfma_f32_16x16x32_f16 v[50:53], v[110:113], v[102:105], v[50:53]
	v_mfma_f32_16x16x32_f16 v[54:57], v[114:117], v[102:105], v[54:57]
	v_mfma_f32_16x16x32_f16 v[42:45], v[118:121], v[102:105], v[42:45]
	v_mfma_f32_16x16x32_f16 v[58:61], v[110:113], v[106:109], v[58:61]
	v_mfma_f32_16x16x32_f16 v[22:25], v[114:117], v[106:109], v[22:25]
	v_mfma_f32_16x16x32_f16 v[30:33], v[118:121], v[106:109], v[30:33]
	v_add_u32_e32 v21, s19, v122
	s_add_u32 s20, s0, 0x280
	v_readfirstlane_b32 s23, v21
	v_add_u32_e32 v98, 0x2000, v21
	s_waitcnt vmcnt(5) lgkmcnt(0)
	s_barrier
	s_addc_u32 s21, s1, 0
	s_mov_b32 m0, s23
	v_readfirstlane_b32 s19, v98
	global_load_lds_dwordx4 v1, s[20:21]
	s_mov_b32 m0, s19
	v_add_u32_e32 v98, 0x4000, v21
	s_add_u32 s24, s2, 0x280
	global_load_lds_dwordx4 v2, s[20:21]
	v_readfirstlane_b32 s20, v98
	v_add_u32_e32 v98, 0x6000, v21
	s_addc_u32 s25, s3, 0
	s_mov_b32 m0, s20
	v_readfirstlane_b32 s21, v98
	v_add_u32_e32 v21, 0x8000, v21
	global_load_lds_dwordx4 v1, s[24:25]
	s_mov_b32 m0, s21
	v_readfirstlane_b32 s22, v21
	global_load_lds_dwordx4 v2, s[24:25]
	s_mov_b32 m0, s22
	s_nop 0
	global_load_lds_dwordx4 v3, s[24:25]
	s_waitcnt lgkmcnt(0)
	v_mfma_f32_16x16x32_f16 v[34:37], v[74:77], v[90:93], v[34:37]
	v_mfma_f32_16x16x32_f16 v[38:41], v[86:89], v[90:93], v[38:41]
	v_mfma_f32_16x16x32_f16 v[46:49], v[94:97], v[90:93], v[46:49]
	ds_read_b128 v[90:93], v6
	ds_read_b128 v[98:101], v6 offset:2048
	ds_read_b128 v[102:105], v6 offset:4096
	ds_read_b128 v[106:109], v6 offset:6144
	ds_read_b128 v[110:113], v4 offset:16384
	ds_read_b128 v[114:117], v4 offset:18432
	ds_read_b128 v[118:121], v4 offset:20480
	v_mfma_f32_16x16x32_f16 v[78:81], v[74:77], v[62:65], v[78:81]
	v_mfma_f32_16x16x32_f16 v[82:85], v[86:89], v[62:65], v[82:85]
	v_mfma_f32_16x16x32_f16 v[26:29], v[94:97], v[62:65], v[26:29]
	v_mfma_f32_16x16x32_f16 v[50:53], v[74:77], v[66:69], v[50:53]
	v_mfma_f32_16x16x32_f16 v[54:57], v[86:89], v[66:69], v[54:57]
	v_mfma_f32_16x16x32_f16 v[42:45], v[94:97], v[66:69], v[42:45]
	v_mfma_f32_16x16x32_f16 v[58:61], v[74:77], v[70:73], v[58:61]
	v_mfma_f32_16x16x32_f16 v[22:25], v[86:89], v[70:73], v[22:25]
	v_mfma_f32_16x16x32_f16 v[30:33], v[94:97], v[70:73], v[30:33]
	s_waitcnt lgkmcnt(0)
	v_mfma_f32_16x16x32_f16 v[34:37], v[110:113], v[90:93], v[34:37]
	v_mfma_f32_16x16x32_f16 v[38:41], v[114:117], v[90:93], v[38:41]
	v_mfma_f32_16x16x32_f16 v[46:49], v[118:121], v[90:93], v[46:49]
	ds_read_b128 v[62:65], v0
	ds_read_b128 v[66:69], v0 offset:2048
	ds_read_b128 v[70:73], v0 offset:4096
	ds_read_b128 v[74:77], v0 offset:6144
	ds_read_b128 v[86:89], v5 offset:16384
	ds_read_b128 v[90:93], v5 offset:18432
	ds_read_b128 v[94:97], v5 offset:20480
	v_mfma_f32_16x16x32_f16 v[78:81], v[110:113], v[98:101], v[78:81]
	v_mfma_f32_16x16x32_f16 v[82:85], v[114:117], v[98:101], v[82:85]
	v_mfma_f32_16x16x32_f16 v[26:29], v[118:121], v[98:101], v[26:29]
	v_mfma_f32_16x16x32_f16 v[50:53], v[110:113], v[102:105], v[50:53]
	v_mfma_f32_16x16x32_f16 v[54:57], v[114:117], v[102:105], v[54:57]
	v_mfma_f32_16x16x32_f16 v[42:45], v[118:121], v[102:105], v[42:45]
	v_mfma_f32_16x16x32_f16 v[58:61], v[110:113], v[106:109], v[58:61]
	v_mfma_f32_16x16x32_f16 v[22:25], v[114:117], v[106:109], v[22:25]
	v_mfma_f32_16x16x32_f16 v[30:33], v[118:121], v[106:109], v[30:33]
	s_add_u32 s24, s0, 0x300
	s_mov_b32 m0, s13
	s_waitcnt vmcnt(5) lgkmcnt(0)
	s_barrier
	s_addc_u32 s25, s1, 0
	s_add_u32 s26, s2, 0x300
	global_load_lds_dwordx4 v1, s[24:25]
	s_mov_b32 m0, s4
	s_addc_u32 s27, s3, 0
	global_load_lds_dwordx4 v2, s[24:25]
	s_mov_b32 m0, s5
	s_nop 0
	global_load_lds_dwordx4 v1, s[26:27]
	s_mov_b32 m0, s6
	s_nop 0
	global_load_lds_dwordx4 v2, s[26:27]
	s_mov_b32 m0, s7
	s_nop 0
	global_load_lds_dwordx4 v3, s[26:27]
	s_waitcnt lgkmcnt(0)
	v_mfma_f32_16x16x32_f16 v[34:37], v[86:89], v[62:65], v[34:37]
	v_mfma_f32_16x16x32_f16 v[38:41], v[90:93], v[62:65], v[38:41]
	v_mfma_f32_16x16x32_f16 v[46:49], v[94:97], v[62:65], v[46:49]
	ds_read_b128 v[62:65], v6 offset:40960
	ds_read_b128 v[98:101], v6 offset:43008
	ds_read_b128 v[102:105], v6 offset:45056
	ds_read_b128 v[106:109], v6 offset:47104
	ds_read_b128 v[110:113], v4 offset:57344
	ds_read_b128 v[114:117], v4 offset:59392
	ds_read_b128 v[118:121], v4 offset:61440
	v_mfma_f32_16x16x32_f16 v[78:81], v[86:89], v[66:69], v[78:81]
	v_mfma_f32_16x16x32_f16 v[82:85], v[90:93], v[66:69], v[82:85]
	v_mfma_f32_16x16x32_f16 v[26:29], v[94:97], v[66:69], v[26:29]
	v_mfma_f32_16x16x32_f16 v[50:53], v[86:89], v[70:73], v[50:53]
	v_mfma_f32_16x16x32_f16 v[54:57], v[90:93], v[70:73], v[54:57]
	v_mfma_f32_16x16x32_f16 v[42:45], v[94:97], v[70:73], v[42:45]
	v_mfma_f32_16x16x32_f16 v[58:61], v[86:89], v[74:77], v[58:61]
	v_mfma_f32_16x16x32_f16 v[22:25], v[90:93], v[74:77], v[22:25]
	v_mfma_f32_16x16x32_f16 v[30:33], v[94:97], v[74:77], v[30:33]
	s_waitcnt lgkmcnt(0)
	v_mfma_f32_16x16x32_f16 v[34:37], v[110:113], v[62:65], v[34:37]
	v_mfma_f32_16x16x32_f16 v[38:41], v[114:117], v[62:65], v[38:41]
	v_mfma_f32_16x16x32_f16 v[46:49], v[118:121], v[62:65], v[46:49]
	ds_read_b128 v[62:65], v0 offset:40960
	ds_read_b128 v[66:69], v0 offset:43008
	ds_read_b128 v[70:73], v0 offset:45056
	ds_read_b128 v[74:77], v0 offset:47104
	ds_read_b128 v[86:89], v5 offset:57344
	ds_read_b128 v[90:93], v5 offset:59392
	ds_read_b128 v[94:97], v5 offset:61440
	v_mfma_f32_16x16x32_f16 v[78:81], v[110:113], v[98:101], v[78:81]
	v_mfma_f32_16x16x32_f16 v[82:85], v[114:117], v[98:101], v[82:85]
	v_mfma_f32_16x16x32_f16 v[26:29], v[118:121], v[98:101], v[26:29]
	v_mfma_f32_16x16x32_f16 v[50:53], v[110:113], v[102:105], v[50:53]
	v_mfma_f32_16x16x32_f16 v[54:57], v[114:117], v[102:105], v[54:57]
	v_mfma_f32_16x16x32_f16 v[42:45], v[118:121], v[102:105], v[42:45]
	v_mfma_f32_16x16x32_f16 v[58:61], v[110:113], v[106:109], v[58:61]
	v_mfma_f32_16x16x32_f16 v[22:25], v[114:117], v[106:109], v[22:25]
	v_mfma_f32_16x16x32_f16 v[30:33], v[118:121], v[106:109], v[30:33]
	s_add_u32 s24, s0, 0x380
	s_mov_b32 m0, s18
	s_waitcnt vmcnt(5) lgkmcnt(0)
	s_barrier
	s_addc_u32 s25, s1, 0
	s_add_u32 s26, s2, 0x380
	global_load_lds_dwordx4 v1, s[24:25]
	s_mov_b32 m0, s14
	s_addc_u32 s27, s3, 0
	global_load_lds_dwordx4 v2, s[24:25]
	s_mov_b32 m0, s15
	s_nop 0
	global_load_lds_dwordx4 v1, s[26:27]
	s_mov_b32 m0, s16
	s_nop 0
	global_load_lds_dwordx4 v2, s[26:27]
	s_mov_b32 m0, s17
	s_nop 0
	global_load_lds_dwordx4 v3, s[26:27]
	s_waitcnt lgkmcnt(0)
	v_mfma_f32_16x16x32_f16 v[34:37], v[86:89], v[62:65], v[34:37]
	v_mfma_f32_16x16x32_f16 v[38:41], v[90:93], v[62:65], v[38:41]
	v_mfma_f32_16x16x32_f16 v[46:49], v[94:97], v[62:65], v[46:49]
	ds_read_b128 v[62:65], v13
	ds_read_b128 v[98:101], v14
	ds_read_b128 v[102:105], v15
	ds_read_b128 v[106:109], v16
	ds_read_b128 v[110:113], v18
	ds_read_b128 v[114:117], v19
	ds_read_b128 v[118:121], v20
	v_mfma_f32_16x16x32_f16 v[78:81], v[86:89], v[66:69], v[78:81]
	v_mfma_f32_16x16x32_f16 v[82:85], v[90:93], v[66:69], v[82:85]
	v_mfma_f32_16x16x32_f16 v[26:29], v[94:97], v[66:69], v[26:29]
	v_mfma_f32_16x16x32_f16 v[50:53], v[86:89], v[70:73], v[50:53]
	v_mfma_f32_16x16x32_f16 v[54:57], v[90:93], v[70:73], v[54:57]
	v_mfma_f32_16x16x32_f16 v[42:45], v[94:97], v[70:73], v[42:45]
	v_mfma_f32_16x16x32_f16 v[58:61], v[86:89], v[74:77], v[58:61]
	v_mfma_f32_16x16x32_f16 v[22:25], v[90:93], v[74:77], v[22:25]
	v_mfma_f32_16x16x32_f16 v[30:33], v[94:97], v[74:77], v[30:33]
	s_waitcnt lgkmcnt(0)
	v_mfma_f32_16x16x32_f16 v[34:37], v[110:113], v[62:65], v[34:37]
	v_mfma_f32_16x16x32_f16 v[38:41], v[114:117], v[62:65], v[38:41]
	v_mfma_f32_16x16x32_f16 v[46:49], v[118:121], v[62:65], v[46:49]
	ds_read_b128 v[62:65], v17 offset:2048
	ds_read_b128 v[66:69], v17 offset:4096
	ds_read_b128 v[70:73], v17 offset:6144
	ds_read_b128 v[74:77], v7 offset:16384
	ds_read_b128 v[86:89], v7 offset:18432
	ds_read_b128 v[90:93], v17
	ds_read_b128 v[94:97], v7 offset:20480
	v_mfma_f32_16x16x32_f16 v[78:81], v[110:113], v[98:101], v[78:81]
	v_mfma_f32_16x16x32_f16 v[82:85], v[114:117], v[98:101], v[82:85]
	v_mfma_f32_16x16x32_f16 v[26:29], v[118:121], v[98:101], v[26:29]
	v_mfma_f32_16x16x32_f16 v[50:53], v[110:113], v[102:105], v[50:53]
	v_mfma_f32_16x16x32_f16 v[54:57], v[114:117], v[102:105], v[54:57]
	v_mfma_f32_16x16x32_f16 v[42:45], v[118:121], v[102:105], v[42:45]
	v_mfma_f32_16x16x32_f16 v[58:61], v[110:113], v[106:109], v[58:61]
	v_mfma_f32_16x16x32_f16 v[22:25], v[114:117], v[106:109], v[22:25]
	v_mfma_f32_16x16x32_f16 v[30:33], v[118:121], v[106:109], v[30:33]
	s_add_u32 s24, s0, 0x400
	s_mov_b32 m0, s23
	s_waitcnt vmcnt(5) lgkmcnt(0)
	s_barrier
	s_addc_u32 s25, s1, 0
	s_add_u32 s26, s2, 0x400
	global_load_lds_dwordx4 v1, s[24:25]
	s_mov_b32 m0, s19
	s_addc_u32 s27, s3, 0
	global_load_lds_dwordx4 v2, s[24:25]
	s_mov_b32 m0, s20
	s_nop 0
	global_load_lds_dwordx4 v1, s[26:27]
	s_mov_b32 m0, s21
	s_nop 0
	global_load_lds_dwordx4 v2, s[26:27]
	s_mov_b32 m0, s22
	s_nop 0
	global_load_lds_dwordx4 v3, s[26:27]
	s_waitcnt lgkmcnt(0)
	v_mfma_f32_16x16x32_f16 v[34:37], v[74:77], v[90:93], v[34:37]
	v_mfma_f32_16x16x32_f16 v[38:41], v[86:89], v[90:93], v[38:41]
	v_mfma_f32_16x16x32_f16 v[46:49], v[94:97], v[90:93], v[46:49]
	ds_read_b128 v[90:93], v6
	ds_read_b128 v[98:101], v6 offset:2048
	ds_read_b128 v[102:105], v6 offset:4096
	ds_read_b128 v[106:109], v6 offset:6144
	ds_read_b128 v[110:113], v4 offset:16384
	ds_read_b128 v[114:117], v4 offset:18432
	ds_read_b128 v[118:121], v4 offset:20480
	v_mfma_f32_16x16x32_f16 v[78:81], v[74:77], v[62:65], v[78:81]
	v_mfma_f32_16x16x32_f16 v[82:85], v[86:89], v[62:65], v[82:85]
	v_mfma_f32_16x16x32_f16 v[26:29], v[94:97], v[62:65], v[26:29]
	v_mfma_f32_16x16x32_f16 v[50:53], v[74:77], v[66:69], v[50:53]
	v_mfma_f32_16x16x32_f16 v[54:57], v[86:89], v[66:69], v[54:57]
	v_mfma_f32_16x16x32_f16 v[42:45], v[94:97], v[66:69], v[42:45]
	v_mfma_f32_16x16x32_f16 v[58:61], v[74:77], v[70:73], v[58:61]
	v_mfma_f32_16x16x32_f16 v[22:25], v[86:89], v[70:73], v[22:25]
	v_mfma_f32_16x16x32_f16 v[30:33], v[94:97], v[70:73], v[30:33]
	s_waitcnt lgkmcnt(0)
	v_mfma_f32_16x16x32_f16 v[34:37], v[110:113], v[90:93], v[34:37]
	v_mfma_f32_16x16x32_f16 v[38:41], v[114:117], v[90:93], v[38:41]
	v_mfma_f32_16x16x32_f16 v[46:49], v[118:121], v[90:93], v[46:49]
	ds_read_b128 v[62:65], v0
	ds_read_b128 v[66:69], v0 offset:2048
	ds_read_b128 v[70:73], v0 offset:4096
	ds_read_b128 v[74:77], v0 offset:6144
	ds_read_b128 v[86:89], v5 offset:16384
	ds_read_b128 v[90:93], v5 offset:18432
	ds_read_b128 v[94:97], v5 offset:20480
	v_mfma_f32_16x16x32_f16 v[78:81], v[110:113], v[98:101], v[78:81]
	v_mfma_f32_16x16x32_f16 v[82:85], v[114:117], v[98:101], v[82:85]
	v_mfma_f32_16x16x32_f16 v[26:29], v[118:121], v[98:101], v[26:29]
	v_mfma_f32_16x16x32_f16 v[50:53], v[110:113], v[102:105], v[50:53]
	v_mfma_f32_16x16x32_f16 v[54:57], v[114:117], v[102:105], v[54:57]
	v_mfma_f32_16x16x32_f16 v[42:45], v[118:121], v[102:105], v[42:45]
	v_mfma_f32_16x16x32_f16 v[58:61], v[110:113], v[106:109], v[58:61]
	v_mfma_f32_16x16x32_f16 v[22:25], v[114:117], v[106:109], v[22:25]
	v_mfma_f32_16x16x32_f16 v[30:33], v[118:121], v[106:109], v[30:33]
	s_add_u32 s24, s0, 0x480
	s_mov_b32 m0, s13
	s_waitcnt vmcnt(5) lgkmcnt(0)
	s_barrier
	s_addc_u32 s25, s1, 0
	s_add_u32 s26, s2, 0x480
	global_load_lds_dwordx4 v1, s[24:25]
	s_mov_b32 m0, s4
	s_addc_u32 s27, s3, 0
	global_load_lds_dwordx4 v2, s[24:25]
	s_mov_b32 m0, s5
	s_nop 0
	global_load_lds_dwordx4 v1, s[26:27]
	s_mov_b32 m0, s6
	s_nop 0
	global_load_lds_dwordx4 v2, s[26:27]
	s_mov_b32 m0, s7
	s_nop 0
	global_load_lds_dwordx4 v3, s[26:27]
	s_waitcnt lgkmcnt(0)
	v_mfma_f32_16x16x32_f16 v[34:37], v[86:89], v[62:65], v[34:37]
	v_mfma_f32_16x16x32_f16 v[38:41], v[90:93], v[62:65], v[38:41]
	v_mfma_f32_16x16x32_f16 v[46:49], v[94:97], v[62:65], v[46:49]
	ds_read_b128 v[62:65], v6 offset:40960
	ds_read_b128 v[98:101], v6 offset:43008
	ds_read_b128 v[102:105], v6 offset:45056
	ds_read_b128 v[106:109], v6 offset:47104
	ds_read_b128 v[110:113], v4 offset:57344
	ds_read_b128 v[114:117], v4 offset:59392
	ds_read_b128 v[118:121], v4 offset:61440
	v_mfma_f32_16x16x32_f16 v[78:81], v[86:89], v[66:69], v[78:81]
	v_mfma_f32_16x16x32_f16 v[82:85], v[90:93], v[66:69], v[82:85]
	v_mfma_f32_16x16x32_f16 v[26:29], v[94:97], v[66:69], v[26:29]
	v_mfma_f32_16x16x32_f16 v[50:53], v[86:89], v[70:73], v[50:53]
	v_mfma_f32_16x16x32_f16 v[54:57], v[90:93], v[70:73], v[54:57]
	v_mfma_f32_16x16x32_f16 v[42:45], v[94:97], v[70:73], v[42:45]
	v_mfma_f32_16x16x32_f16 v[58:61], v[86:89], v[74:77], v[58:61]
	v_mfma_f32_16x16x32_f16 v[22:25], v[90:93], v[74:77], v[22:25]
	v_mfma_f32_16x16x32_f16 v[30:33], v[94:97], v[74:77], v[30:33]
	s_waitcnt lgkmcnt(0)
	v_mfma_f32_16x16x32_f16 v[34:37], v[110:113], v[62:65], v[34:37]
	v_mfma_f32_16x16x32_f16 v[38:41], v[114:117], v[62:65], v[38:41]
	v_mfma_f32_16x16x32_f16 v[46:49], v[118:121], v[62:65], v[46:49]
	ds_read_b128 v[62:65], v0 offset:40960
	ds_read_b128 v[66:69], v0 offset:43008
	ds_read_b128 v[70:73], v0 offset:45056
	ds_read_b128 v[74:77], v0 offset:47104
	ds_read_b128 v[86:89], v5 offset:57344
	ds_read_b128 v[90:93], v5 offset:59392
	ds_read_b128 v[94:97], v5 offset:61440
	v_mfma_f32_16x16x32_f16 v[78:81], v[110:113], v[98:101], v[78:81]
	v_mfma_f32_16x16x32_f16 v[82:85], v[114:117], v[98:101], v[82:85]
	v_mfma_f32_16x16x32_f16 v[26:29], v[118:121], v[98:101], v[26:29]
	v_mfma_f32_16x16x32_f16 v[50:53], v[110:113], v[102:105], v[50:53]
	v_mfma_f32_16x16x32_f16 v[54:57], v[114:117], v[102:105], v[54:57]
	v_mfma_f32_16x16x32_f16 v[42:45], v[118:121], v[102:105], v[42:45]
	v_mfma_f32_16x16x32_f16 v[58:61], v[110:113], v[106:109], v[58:61]
	v_mfma_f32_16x16x32_f16 v[22:25], v[114:117], v[106:109], v[22:25]
	v_mfma_f32_16x16x32_f16 v[30:33], v[118:121], v[106:109], v[30:33]
	s_add_u32 s24, s0, 0x500
	s_mov_b32 m0, s18
	s_waitcnt vmcnt(5) lgkmcnt(0)
	s_barrier
	s_addc_u32 s25, s1, 0
	s_add_u32 s26, s2, 0x500
	global_load_lds_dwordx4 v1, s[24:25]
	s_mov_b32 m0, s14
	s_addc_u32 s27, s3, 0
	global_load_lds_dwordx4 v2, s[24:25]
	s_mov_b32 m0, s15
	s_nop 0
	global_load_lds_dwordx4 v1, s[26:27]
	s_mov_b32 m0, s16
	s_nop 0
	global_load_lds_dwordx4 v2, s[26:27]
	s_mov_b32 m0, s17
	s_nop 0
	global_load_lds_dwordx4 v3, s[26:27]
	s_waitcnt lgkmcnt(0)
	v_mfma_f32_16x16x32_f16 v[34:37], v[86:89], v[62:65], v[34:37]
	v_mfma_f32_16x16x32_f16 v[38:41], v[90:93], v[62:65], v[38:41]
	v_mfma_f32_16x16x32_f16 v[46:49], v[94:97], v[62:65], v[46:49]
	ds_read_b128 v[62:65], v13
	ds_read_b128 v[98:101], v14
	ds_read_b128 v[102:105], v15
	ds_read_b128 v[106:109], v16
	ds_read_b128 v[110:113], v18
	ds_read_b128 v[114:117], v19
	ds_read_b128 v[118:121], v20
	v_mfma_f32_16x16x32_f16 v[78:81], v[86:89], v[66:69], v[78:81]
	v_mfma_f32_16x16x32_f16 v[82:85], v[90:93], v[66:69], v[82:85]
	v_mfma_f32_16x16x32_f16 v[26:29], v[94:97], v[66:69], v[26:29]
	v_mfma_f32_16x16x32_f16 v[50:53], v[86:89], v[70:73], v[50:53]
	v_mfma_f32_16x16x32_f16 v[54:57], v[90:93], v[70:73], v[54:57]
	v_mfma_f32_16x16x32_f16 v[42:45], v[94:97], v[70:73], v[42:45]
	v_mfma_f32_16x16x32_f16 v[58:61], v[86:89], v[74:77], v[58:61]
	v_mfma_f32_16x16x32_f16 v[22:25], v[90:93], v[74:77], v[22:25]
	v_mfma_f32_16x16x32_f16 v[30:33], v[94:97], v[74:77], v[30:33]
	s_waitcnt lgkmcnt(0)
	v_mfma_f32_16x16x32_f16 v[34:37], v[110:113], v[62:65], v[34:37]
	v_mfma_f32_16x16x32_f16 v[38:41], v[114:117], v[62:65], v[38:41]
	v_mfma_f32_16x16x32_f16 v[46:49], v[118:121], v[62:65], v[46:49]
	ds_read_b128 v[62:65], v17 offset:2048
	ds_read_b128 v[66:69], v17 offset:4096
	ds_read_b128 v[70:73], v17 offset:6144
	ds_read_b128 v[74:77], v7 offset:16384
	ds_read_b128 v[86:89], v7 offset:18432
	ds_read_b128 v[90:93], v17
	ds_read_b128 v[94:97], v7 offset:20480
	v_mfma_f32_16x16x32_f16 v[78:81], v[110:113], v[98:101], v[78:81]
	v_mfma_f32_16x16x32_f16 v[82:85], v[114:117], v[98:101], v[82:85]
	v_mfma_f32_16x16x32_f16 v[26:29], v[118:121], v[98:101], v[26:29]
	v_mfma_f32_16x16x32_f16 v[50:53], v[110:113], v[102:105], v[50:53]
	v_mfma_f32_16x16x32_f16 v[54:57], v[114:117], v[102:105], v[54:57]
	v_mfma_f32_16x16x32_f16 v[42:45], v[118:121], v[102:105], v[42:45]
	v_mfma_f32_16x16x32_f16 v[58:61], v[110:113], v[106:109], v[58:61]
	v_mfma_f32_16x16x32_f16 v[22:25], v[114:117], v[106:109], v[22:25]
	v_mfma_f32_16x16x32_f16 v[30:33], v[118:121], v[106:109], v[30:33]
	s_add_u32 s24, s0, 0x580
	s_mov_b32 m0, s23
	s_waitcnt vmcnt(5) lgkmcnt(0)
	s_barrier
	s_addc_u32 s25, s1, 0
	s_add_u32 s26, s2, 0x580
	global_load_lds_dwordx4 v1, s[24:25]
	s_mov_b32 m0, s19
	s_addc_u32 s27, s3, 0
	global_load_lds_dwordx4 v2, s[24:25]
	s_mov_b32 m0, s20
	s_nop 0
	global_load_lds_dwordx4 v1, s[26:27]
	s_mov_b32 m0, s21
	s_nop 0
	global_load_lds_dwordx4 v2, s[26:27]
	s_mov_b32 m0, s22
	s_nop 0
	global_load_lds_dwordx4 v3, s[26:27]
	s_waitcnt lgkmcnt(0)
	v_mfma_f32_16x16x32_f16 v[34:37], v[74:77], v[90:93], v[34:37]
	v_mfma_f32_16x16x32_f16 v[38:41], v[86:89], v[90:93], v[38:41]
	v_mfma_f32_16x16x32_f16 v[46:49], v[94:97], v[90:93], v[46:49]
	ds_read_b128 v[90:93], v6
	ds_read_b128 v[98:101], v6 offset:2048
	ds_read_b128 v[102:105], v6 offset:4096
	ds_read_b128 v[106:109], v6 offset:6144
	ds_read_b128 v[110:113], v4 offset:16384
	ds_read_b128 v[114:117], v4 offset:18432
	ds_read_b128 v[118:121], v4 offset:20480
	v_mfma_f32_16x16x32_f16 v[78:81], v[74:77], v[62:65], v[78:81]
	v_mfma_f32_16x16x32_f16 v[82:85], v[86:89], v[62:65], v[82:85]
	v_mfma_f32_16x16x32_f16 v[26:29], v[94:97], v[62:65], v[26:29]
	v_mfma_f32_16x16x32_f16 v[50:53], v[74:77], v[66:69], v[50:53]
	v_mfma_f32_16x16x32_f16 v[54:57], v[86:89], v[66:69], v[54:57]
	v_mfma_f32_16x16x32_f16 v[42:45], v[94:97], v[66:69], v[42:45]
	v_mfma_f32_16x16x32_f16 v[58:61], v[74:77], v[70:73], v[58:61]
	v_mfma_f32_16x16x32_f16 v[22:25], v[86:89], v[70:73], v[22:25]
	v_mfma_f32_16x16x32_f16 v[30:33], v[94:97], v[70:73], v[30:33]
	s_waitcnt lgkmcnt(0)
	v_mfma_f32_16x16x32_f16 v[34:37], v[110:113], v[90:93], v[34:37]
	v_mfma_f32_16x16x32_f16 v[38:41], v[114:117], v[90:93], v[38:41]
	v_mfma_f32_16x16x32_f16 v[46:49], v[118:121], v[90:93], v[46:49]
	ds_read_b128 v[62:65], v0
	ds_read_b128 v[66:69], v0 offset:2048
	ds_read_b128 v[70:73], v0 offset:4096
	ds_read_b128 v[74:77], v0 offset:6144
	ds_read_b128 v[86:89], v5 offset:16384
	ds_read_b128 v[90:93], v5 offset:18432
	ds_read_b128 v[94:97], v5 offset:20480
	v_mfma_f32_16x16x32_f16 v[78:81], v[110:113], v[98:101], v[78:81]
	v_mfma_f32_16x16x32_f16 v[82:85], v[114:117], v[98:101], v[82:85]
	v_mfma_f32_16x16x32_f16 v[26:29], v[118:121], v[98:101], v[26:29]
	v_mfma_f32_16x16x32_f16 v[50:53], v[110:113], v[102:105], v[50:53]
	v_mfma_f32_16x16x32_f16 v[54:57], v[114:117], v[102:105], v[54:57]
	v_mfma_f32_16x16x32_f16 v[42:45], v[118:121], v[102:105], v[42:45]
	v_mfma_f32_16x16x32_f16 v[58:61], v[110:113], v[106:109], v[58:61]
	v_mfma_f32_16x16x32_f16 v[22:25], v[114:117], v[106:109], v[22:25]
	v_mfma_f32_16x16x32_f16 v[30:33], v[118:121], v[106:109], v[30:33]
	s_add_u32 s24, s0, 0x600
	s_mov_b32 m0, s13
	s_waitcnt vmcnt(5) lgkmcnt(0)
	s_barrier
	s_addc_u32 s25, s1, 0
	s_add_u32 s26, s2, 0x600
	global_load_lds_dwordx4 v1, s[24:25]
	s_mov_b32 m0, s4
	s_addc_u32 s27, s3, 0
	global_load_lds_dwordx4 v2, s[24:25]
	s_mov_b32 m0, s5
	s_nop 0
	global_load_lds_dwordx4 v1, s[26:27]
	s_mov_b32 m0, s6
	s_nop 0
	global_load_lds_dwordx4 v2, s[26:27]
	s_mov_b32 m0, s7
	s_nop 0
	global_load_lds_dwordx4 v3, s[26:27]
	s_waitcnt lgkmcnt(0)
	v_mfma_f32_16x16x32_f16 v[34:37], v[86:89], v[62:65], v[34:37]
	v_mfma_f32_16x16x32_f16 v[38:41], v[90:93], v[62:65], v[38:41]
	v_mfma_f32_16x16x32_f16 v[46:49], v[94:97], v[62:65], v[46:49]
	ds_read_b128 v[62:65], v6 offset:40960
	ds_read_b128 v[98:101], v6 offset:43008
	ds_read_b128 v[102:105], v6 offset:45056
	ds_read_b128 v[106:109], v6 offset:47104
	ds_read_b128 v[110:113], v4 offset:57344
	ds_read_b128 v[114:117], v4 offset:59392
	ds_read_b128 v[118:121], v4 offset:61440
	v_mfma_f32_16x16x32_f16 v[78:81], v[86:89], v[66:69], v[78:81]
	v_mfma_f32_16x16x32_f16 v[82:85], v[90:93], v[66:69], v[82:85]
	v_mfma_f32_16x16x32_f16 v[26:29], v[94:97], v[66:69], v[26:29]
	v_mfma_f32_16x16x32_f16 v[50:53], v[86:89], v[70:73], v[50:53]
	v_mfma_f32_16x16x32_f16 v[54:57], v[90:93], v[70:73], v[54:57]
	v_mfma_f32_16x16x32_f16 v[42:45], v[94:97], v[70:73], v[42:45]
	v_mfma_f32_16x16x32_f16 v[58:61], v[86:89], v[74:77], v[58:61]
	v_mfma_f32_16x16x32_f16 v[22:25], v[90:93], v[74:77], v[22:25]
	v_mfma_f32_16x16x32_f16 v[30:33], v[94:97], v[74:77], v[30:33]
	s_waitcnt lgkmcnt(0)
	v_mfma_f32_16x16x32_f16 v[34:37], v[110:113], v[62:65], v[34:37]
	v_mfma_f32_16x16x32_f16 v[38:41], v[114:117], v[62:65], v[38:41]
	v_mfma_f32_16x16x32_f16 v[46:49], v[118:121], v[62:65], v[46:49]
	ds_read_b128 v[62:65], v0 offset:40960
	ds_read_b128 v[66:69], v0 offset:43008
	ds_read_b128 v[70:73], v0 offset:45056
	ds_read_b128 v[74:77], v0 offset:47104
	ds_read_b128 v[86:89], v5 offset:57344
	ds_read_b128 v[90:93], v5 offset:59392
	ds_read_b128 v[94:97], v5 offset:61440
	v_mfma_f32_16x16x32_f16 v[78:81], v[110:113], v[98:101], v[78:81]
	v_mfma_f32_16x16x32_f16 v[82:85], v[114:117], v[98:101], v[82:85]
	v_mfma_f32_16x16x32_f16 v[26:29], v[118:121], v[98:101], v[26:29]
	v_mfma_f32_16x16x32_f16 v[50:53], v[110:113], v[102:105], v[50:53]
	v_mfma_f32_16x16x32_f16 v[54:57], v[114:117], v[102:105], v[54:57]
	v_mfma_f32_16x16x32_f16 v[42:45], v[118:121], v[102:105], v[42:45]
	v_mfma_f32_16x16x32_f16 v[58:61], v[110:113], v[106:109], v[58:61]
	v_mfma_f32_16x16x32_f16 v[22:25], v[114:117], v[106:109], v[22:25]
	v_mfma_f32_16x16x32_f16 v[30:33], v[118:121], v[106:109], v[30:33]
	s_add_u32 s24, s0, 0x680
	s_mov_b32 m0, s18
	s_waitcnt vmcnt(5) lgkmcnt(0)
	s_barrier
	s_addc_u32 s25, s1, 0
	s_add_u32 s26, s2, 0x680
	global_load_lds_dwordx4 v1, s[24:25]
	s_mov_b32 m0, s14
	s_addc_u32 s27, s3, 0
	global_load_lds_dwordx4 v2, s[24:25]
	s_mov_b32 m0, s15
	s_nop 0
	global_load_lds_dwordx4 v1, s[26:27]
	s_mov_b32 m0, s16
	s_nop 0
	global_load_lds_dwordx4 v2, s[26:27]
	s_mov_b32 m0, s17
	s_nop 0
	global_load_lds_dwordx4 v3, s[26:27]
	s_waitcnt lgkmcnt(0)
	v_mfma_f32_16x16x32_f16 v[34:37], v[86:89], v[62:65], v[34:37]
	v_mfma_f32_16x16x32_f16 v[38:41], v[90:93], v[62:65], v[38:41]
	v_mfma_f32_16x16x32_f16 v[46:49], v[94:97], v[62:65], v[46:49]
	ds_read_b128 v[62:65], v13
	ds_read_b128 v[98:101], v14
	ds_read_b128 v[102:105], v15
	ds_read_b128 v[106:109], v16
	ds_read_b128 v[110:113], v18
	ds_read_b128 v[114:117], v19
	ds_read_b128 v[118:121], v20
	v_mfma_f32_16x16x32_f16 v[78:81], v[86:89], v[66:69], v[78:81]
	v_mfma_f32_16x16x32_f16 v[82:85], v[90:93], v[66:69], v[82:85]
	v_mfma_f32_16x16x32_f16 v[26:29], v[94:97], v[66:69], v[26:29]
	v_mfma_f32_16x16x32_f16 v[50:53], v[86:89], v[70:73], v[50:53]
	v_mfma_f32_16x16x32_f16 v[54:57], v[90:93], v[70:73], v[54:57]
	v_mfma_f32_16x16x32_f16 v[42:45], v[94:97], v[70:73], v[42:45]
	v_mfma_f32_16x16x32_f16 v[58:61], v[86:89], v[74:77], v[58:61]
	v_mfma_f32_16x16x32_f16 v[22:25], v[90:93], v[74:77], v[22:25]
	v_mfma_f32_16x16x32_f16 v[30:33], v[94:97], v[74:77], v[30:33]
	s_waitcnt lgkmcnt(0)
	v_mfma_f32_16x16x32_f16 v[34:37], v[110:113], v[62:65], v[34:37]
	v_mfma_f32_16x16x32_f16 v[38:41], v[114:117], v[62:65], v[38:41]
	v_mfma_f32_16x16x32_f16 v[46:49], v[118:121], v[62:65], v[46:49]
	ds_read_b128 v[62:65], v17 offset:2048
	ds_read_b128 v[66:69], v17 offset:4096
	ds_read_b128 v[70:73], v17 offset:6144
	ds_read_b128 v[74:77], v7 offset:16384
	ds_read_b128 v[86:89], v7 offset:18432
	ds_read_b128 v[90:93], v17
	ds_read_b128 v[94:97], v7 offset:20480
	v_mfma_f32_16x16x32_f16 v[78:81], v[110:113], v[98:101], v[78:81]
	v_mfma_f32_16x16x32_f16 v[82:85], v[114:117], v[98:101], v[82:85]
	v_mfma_f32_16x16x32_f16 v[26:29], v[118:121], v[98:101], v[26:29]
	v_mfma_f32_16x16x32_f16 v[50:53], v[110:113], v[102:105], v[50:53]
	v_mfma_f32_16x16x32_f16 v[54:57], v[114:117], v[102:105], v[54:57]
	v_mfma_f32_16x16x32_f16 v[42:45], v[118:121], v[102:105], v[42:45]
	v_mfma_f32_16x16x32_f16 v[58:61], v[110:113], v[106:109], v[58:61]
	v_mfma_f32_16x16x32_f16 v[22:25], v[114:117], v[106:109], v[22:25]
	v_mfma_f32_16x16x32_f16 v[30:33], v[118:121], v[106:109], v[30:33]
	s_add_u32 s14, s0, 0x700
	s_mov_b32 m0, s23
	s_waitcnt vmcnt(5) lgkmcnt(0)
	s_barrier
	s_addc_u32 s15, s1, 0
	s_add_u32 s16, s2, 0x700
	global_load_lds_dwordx4 v1, s[14:15]
	s_mov_b32 m0, s19
	s_addc_u32 s17, s3, 0
	global_load_lds_dwordx4 v2, s[14:15]
	s_mov_b32 m0, s20
	s_nop 0
	global_load_lds_dwordx4 v1, s[16:17]
	s_mov_b32 m0, s21
	s_nop 0
	global_load_lds_dwordx4 v2, s[16:17]
	s_mov_b32 m0, s22
	s_nop 0
	global_load_lds_dwordx4 v3, s[16:17]
	s_waitcnt lgkmcnt(0)
	v_mfma_f32_16x16x32_f16 v[34:37], v[74:77], v[90:93], v[34:37]
	v_mfma_f32_16x16x32_f16 v[38:41], v[86:89], v[90:93], v[38:41]
	v_mfma_f32_16x16x32_f16 v[46:49], v[94:97], v[90:93], v[46:49]
	ds_read_b128 v[90:93], v6
	ds_read_b128 v[98:101], v6 offset:2048
	ds_read_b128 v[102:105], v6 offset:4096
	ds_read_b128 v[106:109], v6 offset:6144
	ds_read_b128 v[110:113], v4 offset:16384
	ds_read_b128 v[114:117], v4 offset:18432
	ds_read_b128 v[118:121], v4 offset:20480
	v_mfma_f32_16x16x32_f16 v[78:81], v[74:77], v[62:65], v[78:81]
	v_mfma_f32_16x16x32_f16 v[82:85], v[86:89], v[62:65], v[82:85]
	v_mfma_f32_16x16x32_f16 v[26:29], v[94:97], v[62:65], v[26:29]
	v_mfma_f32_16x16x32_f16 v[50:53], v[74:77], v[66:69], v[50:53]
	v_mfma_f32_16x16x32_f16 v[54:57], v[86:89], v[66:69], v[54:57]
	v_mfma_f32_16x16x32_f16 v[42:45], v[94:97], v[66:69], v[42:45]
	v_mfma_f32_16x16x32_f16 v[58:61], v[74:77], v[70:73], v[58:61]
	v_mfma_f32_16x16x32_f16 v[22:25], v[86:89], v[70:73], v[22:25]
	v_mfma_f32_16x16x32_f16 v[30:33], v[94:97], v[70:73], v[30:33]
	s_waitcnt lgkmcnt(0)
	v_mfma_f32_16x16x32_f16 v[34:37], v[110:113], v[90:93], v[34:37]
	v_mfma_f32_16x16x32_f16 v[38:41], v[114:117], v[90:93], v[38:41]
	v_mfma_f32_16x16x32_f16 v[46:49], v[118:121], v[90:93], v[46:49]
	ds_read_b128 v[62:65], v0
	ds_read_b128 v[66:69], v0 offset:2048
	ds_read_b128 v[70:73], v0 offset:4096
	ds_read_b128 v[74:77], v0 offset:6144
	ds_read_b128 v[86:89], v5 offset:16384
	ds_read_b128 v[90:93], v5 offset:18432
	ds_read_b128 v[94:97], v5 offset:20480
	v_mfma_f32_16x16x32_f16 v[78:81], v[110:113], v[98:101], v[78:81]
	v_mfma_f32_16x16x32_f16 v[82:85], v[114:117], v[98:101], v[82:85]
	v_mfma_f32_16x16x32_f16 v[26:29], v[118:121], v[98:101], v[26:29]
	v_mfma_f32_16x16x32_f16 v[50:53], v[110:113], v[102:105], v[50:53]
	v_mfma_f32_16x16x32_f16 v[54:57], v[114:117], v[102:105], v[54:57]
	v_mfma_f32_16x16x32_f16 v[42:45], v[118:121], v[102:105], v[42:45]
	v_mfma_f32_16x16x32_f16 v[58:61], v[110:113], v[106:109], v[58:61]
	v_mfma_f32_16x16x32_f16 v[22:25], v[114:117], v[106:109], v[22:25]
	v_mfma_f32_16x16x32_f16 v[30:33], v[118:121], v[106:109], v[30:33]
	s_add_u32 s0, s0, 0x780
	s_mov_b32 m0, s13
	s_waitcnt vmcnt(5) lgkmcnt(0)
	s_barrier
	s_addc_u32 s1, s1, 0
	s_add_u32 s2, s2, 0x780
	global_load_lds_dwordx4 v1, s[0:1]
	s_mov_b32 m0, s4
	s_addc_u32 s3, s3, 0
	global_load_lds_dwordx4 v2, s[0:1]
	s_mov_b32 m0, s5
	s_nop 0
	global_load_lds_dwordx4 v1, s[2:3]
	s_mov_b32 m0, s6
	s_nop 0
	global_load_lds_dwordx4 v2, s[2:3]
	s_mov_b32 m0, s7
	s_nop 0
	global_load_lds_dwordx4 v3, s[2:3]
	s_waitcnt lgkmcnt(0)
	v_mfma_f32_16x16x32_f16 v[34:37], v[86:89], v[62:65], v[34:37]
	v_mfma_f32_16x16x32_f16 v[38:41], v[90:93], v[62:65], v[38:41]
	v_mfma_f32_16x16x32_f16 v[46:49], v[94:97], v[62:65], v[46:49]
	ds_read_b128 v[62:65], v6 offset:40960
	ds_read_b128 v[98:101], v6 offset:43008
	ds_read_b128 v[102:105], v6 offset:45056
	ds_read_b128 v[106:109], v6 offset:47104
	ds_read_b128 v[110:113], v4 offset:57344
	ds_read_b128 v[114:117], v4 offset:59392
	ds_read_b128 v[118:121], v4 offset:61440
	v_mfma_f32_16x16x32_f16 v[78:81], v[86:89], v[66:69], v[78:81]
	v_mfma_f32_16x16x32_f16 v[82:85], v[90:93], v[66:69], v[82:85]
	v_mfma_f32_16x16x32_f16 v[26:29], v[94:97], v[66:69], v[26:29]
	v_mfma_f32_16x16x32_f16 v[50:53], v[86:89], v[70:73], v[50:53]
	v_mfma_f32_16x16x32_f16 v[54:57], v[90:93], v[70:73], v[54:57]
	v_mfma_f32_16x16x32_f16 v[42:45], v[94:97], v[70:73], v[42:45]
	v_mfma_f32_16x16x32_f16 v[58:61], v[86:89], v[74:77], v[58:61]
	v_mfma_f32_16x16x32_f16 v[22:25], v[90:93], v[74:77], v[22:25]
	v_mfma_f32_16x16x32_f16 v[30:33], v[94:97], v[74:77], v[30:33]
	s_waitcnt lgkmcnt(0)
	v_mfma_f32_16x16x32_f16 v[34:37], v[110:113], v[62:65], v[34:37]
	v_mfma_f32_16x16x32_f16 v[38:41], v[114:117], v[62:65], v[38:41]
	v_mfma_f32_16x16x32_f16 v[46:49], v[118:121], v[62:65], v[46:49]
	ds_read_b128 v[62:65], v0 offset:40960
	ds_read_b128 v[66:69], v0 offset:43008
	ds_read_b128 v[70:73], v0 offset:45056
	ds_read_b128 v[74:77], v0 offset:47104
	ds_read_b128 v[86:89], v5 offset:57344
	ds_read_b128 v[90:93], v5 offset:59392
	ds_read_b128 v[94:97], v5 offset:61440
	v_mfma_f32_16x16x32_f16 v[78:81], v[110:113], v[98:101], v[78:81]
	v_mfma_f32_16x16x32_f16 v[82:85], v[114:117], v[98:101], v[82:85]
	v_mfma_f32_16x16x32_f16 v[26:29], v[118:121], v[98:101], v[26:29]
	v_mfma_f32_16x16x32_f16 v[50:53], v[110:113], v[102:105], v[50:53]
	v_mfma_f32_16x16x32_f16 v[54:57], v[114:117], v[102:105], v[54:57]
	v_mfma_f32_16x16x32_f16 v[42:45], v[118:121], v[102:105], v[42:45]
	v_mfma_f32_16x16x32_f16 v[58:61], v[110:113], v[106:109], v[58:61]
	v_mfma_f32_16x16x32_f16 v[22:25], v[114:117], v[106:109], v[22:25]
	v_mfma_f32_16x16x32_f16 v[30:33], v[118:121], v[106:109], v[30:33]
	s_waitcnt vmcnt(5) lgkmcnt(0)
	s_barrier
	s_waitcnt lgkmcnt(0)
	v_mfma_f32_16x16x32_f16 v[34:37], v[86:89], v[62:65], v[34:37]
	v_mfma_f32_16x16x32_f16 v[38:41], v[90:93], v[62:65], v[38:41]
	v_mfma_f32_16x16x32_f16 v[46:49], v[94:97], v[62:65], v[46:49]
	ds_read_b128 v[62:65], v13
	ds_read_b128 v[98:101], v14
	ds_read_b128 v[102:105], v15
	ds_read_b128 v[106:109], v16
	ds_read_b128 v[110:113], v18
	ds_read_b128 v[114:117], v19
	ds_read_b128 v[18:21], v20
	v_mfma_f32_16x16x32_f16 v[78:81], v[86:89], v[66:69], v[78:81]
	v_mfma_f32_16x16x32_f16 v[82:85], v[90:93], v[66:69], v[82:85]
	v_mfma_f32_16x16x32_f16 v[26:29], v[94:97], v[66:69], v[26:29]
	v_mfma_f32_16x16x32_f16 v[50:53], v[86:89], v[70:73], v[50:53]
	v_mfma_f32_16x16x32_f16 v[54:57], v[90:93], v[70:73], v[54:57]
	v_mfma_f32_16x16x32_f16 v[42:45], v[94:97], v[70:73], v[42:45]
	v_mfma_f32_16x16x32_f16 v[58:61], v[86:89], v[74:77], v[58:61]
	v_mfma_f32_16x16x32_f16 v[22:25], v[90:93], v[74:77], v[22:25]
	v_mfma_f32_16x16x32_f16 v[30:33], v[94:97], v[74:77], v[30:33]
	s_waitcnt lgkmcnt(0)
	v_mfma_f32_16x16x32_f16 v[34:37], v[110:113], v[62:65], v[34:37]
	v_mfma_f32_16x16x32_f16 v[38:41], v[114:117], v[62:65], v[38:41]
	v_mfma_f32_16x16x32_f16 v[46:49], v[18:21], v[62:65], v[46:49]
	ds_read_b128 v[62:65], v17 offset:2048
	ds_read_b128 v[66:69], v17 offset:4096
	ds_read_b128 v[70:73], v17 offset:6144
	ds_read_b128 v[74:77], v7 offset:16384
	ds_read_b128 v[86:89], v7 offset:18432
	ds_read_b128 v[14:17], v17
	ds_read_b128 v[90:93], v7 offset:20480
	v_mfma_f32_16x16x32_f16 v[78:81], v[110:113], v[98:101], v[78:81]
	v_mfma_f32_16x16x32_f16 v[82:85], v[114:117], v[98:101], v[82:85]
	v_mfma_f32_16x16x32_f16 v[26:29], v[18:21], v[98:101], v[26:29]
	v_mfma_f32_16x16x32_f16 v[50:53], v[110:113], v[102:105], v[50:53]
	v_mfma_f32_16x16x32_f16 v[54:57], v[114:117], v[102:105], v[54:57]
	v_mfma_f32_16x16x32_f16 v[42:45], v[18:21], v[102:105], v[42:45]
	v_mfma_f32_16x16x32_f16 v[58:61], v[110:113], v[106:109], v[58:61]
	v_mfma_f32_16x16x32_f16 v[22:25], v[114:117], v[106:109], v[22:25]
	v_mfma_f32_16x16x32_f16 v[18:21], v[18:21], v[106:109], v[30:33]
	s_waitcnt vmcnt(0) lgkmcnt(0)
	s_barrier
	s_waitcnt lgkmcnt(0)
	v_mfma_f32_16x16x32_f16 v[30:33], v[74:77], v[14:17], v[34:37]
	v_mfma_f32_16x16x32_f16 v[34:37], v[86:89], v[14:17], v[38:41]
	v_mfma_f32_16x16x32_f16 v[14:17], v[90:93], v[14:17], v[46:49]
	s_nop 1
	ds_read_b128 v[38:41], v6
	ds_read_b128 v[46:49], v6 offset:2048
	ds_read_b128 v[94:97], v6 offset:4096
	ds_read_b128 v[98:101], v6 offset:6144
	ds_read_b128 v[102:105], v4 offset:16384
	ds_read_b128 v[106:109], v4 offset:18432
	ds_read_b128 v[110:113], v4 offset:20480
	v_mfma_f32_16x16x32_f16 v[78:81], v[74:77], v[62:65], v[78:81]
	v_mfma_f32_16x16x32_f16 v[82:85], v[86:89], v[62:65], v[82:85]
	v_mfma_f32_16x16x32_f16 v[26:29], v[90:93], v[62:65], v[26:29]
	v_mfma_f32_16x16x32_f16 v[50:53], v[74:77], v[66:69], v[50:53]
	v_mfma_f32_16x16x32_f16 v[54:57], v[86:89], v[66:69], v[54:57]
	v_mfma_f32_16x16x32_f16 v[42:45], v[90:93], v[66:69], v[42:45]
	v_mfma_f32_16x16x32_f16 v[58:61], v[74:77], v[70:73], v[58:61]
	v_mfma_f32_16x16x32_f16 v[22:25], v[86:89], v[70:73], v[22:25]
	v_mfma_f32_16x16x32_f16 v[18:21], v[90:93], v[70:73], v[18:21]
	s_waitcnt lgkmcnt(0)
	v_mfma_f32_16x16x32_f16 v[30:33], v[102:105], v[38:41], v[30:33]
	v_mfma_f32_16x16x32_f16 v[34:37], v[106:109], v[38:41], v[34:37]
	v_mfma_f32_16x16x32_f16 v[14:17], v[110:113], v[38:41], v[14:17]
	ds_read_b128 v[38:41], v0
	ds_read_b128 v[62:65], v0 offset:2048
	ds_read_b128 v[66:69], v0 offset:4096
	ds_read_b128 v[0:3], v0 offset:6144
	ds_read_b128 v[70:73], v5 offset:16384
	ds_read_b128 v[74:77], v5 offset:18432
	ds_read_b128 v[86:89], v5 offset:20480
	v_mfma_f32_16x16x32_f16 v[4:7], v[102:105], v[46:49], v[78:81]
	v_mfma_f32_16x16x32_f16 v[78:81], v[106:109], v[46:49], v[82:85]
	v_mfma_f32_16x16x32_f16 v[26:29], v[110:113], v[46:49], v[26:29]
	v_mfma_f32_16x16x32_f16 v[46:49], v[102:105], v[94:97], v[50:53]
	v_mfma_f32_16x16x32_f16 v[50:53], v[106:109], v[94:97], v[54:57]
	v_mfma_f32_16x16x32_f16 v[42:45], v[110:113], v[94:97], v[42:45]
	v_mfma_f32_16x16x32_f16 v[54:57], v[102:105], v[98:101], v[58:61]
	v_mfma_f32_16x16x32_f16 v[22:25], v[106:109], v[98:101], v[22:25]
	v_mfma_f32_16x16x32_f16 v[18:21], v[110:113], v[98:101], v[18:21]
	s_waitcnt lgkmcnt(0)
	v_mfma_f32_16x16x32_f16 v[30:33], v[70:73], v[38:41], v[30:33]
	v_mfma_f32_16x16x32_f16 v[34:37], v[74:77], v[38:41], v[34:37]
	v_mfma_f32_16x16x32_f16 v[14:17], v[86:89], v[38:41], v[14:17]
	v_mfma_f32_16x16x32_f16 v[38:41], v[70:73], v[62:65], v[4:7]
	v_mfma_f32_16x16x32_f16 v[58:61], v[74:77], v[62:65], v[78:81]
	v_mfma_f32_16x16x32_f16 v[26:29], v[86:89], v[62:65], v[26:29]
	v_mfma_f32_16x16x32_f16 v[46:49], v[70:73], v[66:69], v[46:49]
	v_mfma_f32_16x16x32_f16 v[50:53], v[74:77], v[66:69], v[50:53]
	v_mfma_f32_16x16x32_f16 v[42:45], v[86:89], v[66:69], v[42:45]
	v_mfma_f32_16x16x32_f16 v[54:57], v[70:73], v[0:3], v[54:57]
	v_mfma_f32_16x16x32_f16 v[4:7], v[74:77], v[0:3], v[22:25]
	v_mfma_f32_16x16x32_f16 v[0:3], v[86:89], v[0:3], v[18:21]
	s_barrier
	v_lshrrev_b32_e32 v64, 6, v11
	v_add_u32_e32 v65, s11, v10
	s_mov_b32 s4, 0x3e38aa3b
	v_lshl_add_u32 v64, v64, 6, v8
	v_mov_b32_e32 v66, 1.0
	v_mov_b32_e32 v67, s4
	s_movk_i32 s0, 0x400
	v_cmp_gt_u32_e32 vcc, s0, v65
	v_mul_u32_u24_e32 v64, 0x190, v64
	s_movk_i32 s1, 0x3f0
	s_nop 0
	v_cndmask_b32_e32 v68, v66, v67, vcc
	v_cmp_gt_u32_e32 vcc, s1, v65
	v_lshl_add_u32 v64, v10, 1, v64
	s_movk_i32 s0, 0x3e0
	s_nop 0
	v_cndmask_b32_e32 v70, v66, v67, vcc
	v_cmp_gt_u32_e32 vcc, s0, v65
	v_lshl_add_u32 v64, v12, 3, v64
	v_and_b32_e32 v74, 3, v8
	s_nop 0
	v_cndmask_b32_e32 v72, v66, v67, vcc
	v_lshl_or_b32 v74, v11, 2, v74
	v_pk_mul_f32 v[30:31], v[30:31], v[68:69] op_sel_hi:[1,0]
	v_pk_mul_f32 v[32:33], v[32:33], v[68:69] op_sel_hi:[1,0]
	v_cvt_pk_f16_f32 v30, v30, v31
	v_cvt_pk_f16_f32 v31, v32, v33
	ds_write_b64 v64, v[30:31]
	v_pk_mul_f32 v[34:35], v[34:35], v[70:71] op_sel_hi:[1,0]
	v_pk_mul_f32 v[36:37], v[36:37], v[70:71] op_sel_hi:[1,0]
	v_cvt_pk_f16_f32 v34, v34, v35
	v_cvt_pk_f16_f32 v35, v36, v37
	ds_write_b64 v64, v[34:35] offset:32
	v_pk_mul_f32 v[14:15], v[14:15], v[72:73] op_sel_hi:[1,0]
	v_pk_mul_f32 v[16:17], v[16:17], v[72:73] op_sel_hi:[1,0]
	v_cvt_pk_f16_f32 v14, v14, v15
	v_cvt_pk_f16_f32 v15, v16, v17
	ds_write_b64 v64, v[14:15] offset:64
	v_pk_mul_f32 v[38:39], v[38:39], v[68:69] op_sel_hi:[1,0]
	v_pk_mul_f32 v[40:41], v[40:41], v[68:69] op_sel_hi:[1,0]
	v_cvt_pk_f16_f32 v38, v38, v39
	v_cvt_pk_f16_f32 v39, v40, v41
	ds_write_b64 v64, v[38:39] offset:6400
	v_pk_mul_f32 v[58:59], v[58:59], v[70:71] op_sel_hi:[1,0]
	v_pk_mul_f32 v[60:61], v[60:61], v[70:71] op_sel_hi:[1,0]
	v_cvt_pk_f16_f32 v58, v58, v59
	v_cvt_pk_f16_f32 v59, v60, v61
	ds_write_b64 v64, v[58:59] offset:6432
	v_pk_mul_f32 v[26:27], v[26:27], v[72:73] op_sel_hi:[1,0]
	v_pk_mul_f32 v[28:29], v[28:29], v[72:73] op_sel_hi:[1,0]
	v_cvt_pk_f16_f32 v26, v26, v27
	v_cvt_pk_f16_f32 v27, v28, v29
	ds_write_b64 v64, v[26:27] offset:6464
	v_pk_mul_f32 v[46:47], v[46:47], v[68:69] op_sel_hi:[1,0]
	v_pk_mul_f32 v[48:49], v[48:49], v[68:69] op_sel_hi:[1,0]
	v_cvt_pk_f16_f32 v46, v46, v47
	v_cvt_pk_f16_f32 v47, v48, v49
	ds_write_b64 v64, v[46:47] offset:12800
	v_pk_mul_f32 v[50:51], v[50:51], v[70:71] op_sel_hi:[1,0]
	v_pk_mul_f32 v[52:53], v[52:53], v[70:71] op_sel_hi:[1,0]
	v_cvt_pk_f16_f32 v50, v50, v51
	v_cvt_pk_f16_f32 v51, v52, v53
	ds_write_b64 v64, v[50:51] offset:12832
	v_pk_mul_f32 v[42:43], v[42:43], v[72:73] op_sel_hi:[1,0]
	v_pk_mul_f32 v[44:45], v[44:45], v[72:73] op_sel_hi:[1,0]
	v_cvt_pk_f16_f32 v42, v42, v43
	v_cvt_pk_f16_f32 v43, v44, v45
	ds_write_b64 v64, v[42:43] offset:12864
	v_pk_mul_f32 v[54:55], v[54:55], v[68:69] op_sel_hi:[1,0]
	v_pk_mul_f32 v[56:57], v[56:57], v[68:69] op_sel_hi:[1,0]
	v_cvt_pk_f16_f32 v54, v54, v55
	v_cvt_pk_f16_f32 v55, v56, v57
	ds_write_b64 v64, v[54:55] offset:19200
	v_pk_mul_f32 v[4:5], v[4:5], v[70:71] op_sel_hi:[1,0]
	v_pk_mul_f32 v[6:7], v[6:7], v[70:71] op_sel_hi:[1,0]
	v_cvt_pk_f16_f32 v4, v4, v5
	v_cvt_pk_f16_f32 v5, v6, v7
	ds_write_b64 v64, v[4:5] offset:19232
	v_pk_mul_f32 v[0:1], v[0:1], v[72:73] op_sel_hi:[1,0]
	v_pk_mul_f32 v[2:3], v[2:3], v[72:73] op_sel_hi:[1,0]
	v_cvt_pk_f16_f32 v0, v0, v1
	v_cvt_pk_f16_f32 v1, v2, v3
	ds_write_b64 v64, v[0:1] offset:19264
	v_lshrrev_b32_e32 v75, 3, v74
	v_and_b32_e32 v76, 7, v74
	v_mul_u32_u24_e32 v75, 0x190, v75
	v_lshl_add_u32 v75, v76, 4, v75
	v_lshlrev_b32_e32 v76, 4, v74
	v_add_u32_e32 v77, 0x2000, v76
	s_and_b32 s13, s10, 0x380
	s_lshr_b32 s14, s12, 3
	s_lshl_b32 s14, s14, 4
	s_mov_b32 s15, s11
	s_lshr_b32 s16, s15, 10
	s_bfe_u32 s17, s15, 0x40006
	s_add_u32 s17, s17, s14
	s_lshl_b32 s17, s17, 10
	s_add_u32 s17, s17, s13
	s_lshl_b32 s17, s17, 7
	s_lshl_b32 s16, s16, 22
	s_add_u32 s17, s17, s16
	s_add_u32 s20, s8, s17
	s_addc_u32 s21, s9, 0
	s_add_u32 s15, s11, 64
	s_lshr_b32 s16, s15, 10
	s_bfe_u32 s17, s15, 0x40006
	s_add_u32 s17, s17, s14
	s_lshl_b32 s17, s17, 10
	s_add_u32 s17, s17, s13
	s_lshl_b32 s17, s17, 7
	s_lshl_b32 s16, s16, 22
	s_add_u32 s17, s17, s16
	s_add_u32 s22, s8, s17
	s_addc_u32 s23, s9, 0
	s_add_u32 s15, s11, 128
	s_lshr_b32 s16, s15, 10
	s_bfe_u32 s17, s15, 0x40006
	s_add_u32 s17, s17, s14
	s_lshl_b32 s17, s17, 10
	s_add_u32 s17, s17, s13
	s_lshl_b32 s17, s17, 7
	s_lshl_b32 s16, s16, 22
	s_add_u32 s17, s17, s16
	s_add_u32 s24, s8, s17
	s_addc_u32 s25, s9, 0
	s_waitcnt lgkmcnt(0)
	s_barrier
	ds_read_b128 v[80:83], v75
	ds_read_b128 v[84:87], v75 offset:25600
	ds_read_b128 v[88:91], v75 offset:128
	ds_read_b128 v[92:95], v75 offset:25728
	ds_read_b128 v[96:99], v75 offset:256
	ds_read_b128 v[100:103], v75 offset:25856
	s_waitcnt lgkmcnt(5)
	global_store_dwordx4 v76, v[80:83], s[20:21] sc1
	s_waitcnt lgkmcnt(4)
	global_store_dwordx4 v77, v[84:87], s[20:21] sc1
	s_waitcnt lgkmcnt(3)
	global_store_dwordx4 v76, v[88:91], s[22:23] sc1
	s_waitcnt lgkmcnt(2)
	global_store_dwordx4 v77, v[92:95], s[22:23] sc1
	s_waitcnt lgkmcnt(1)
	global_store_dwordx4 v76, v[96:99], s[24:25] sc1
	s_waitcnt lgkmcnt(0)
	global_store_dwordx4 v77, v[100:103], s[24:25] sc1
	s_endpgm
	s_endpgm
	s_endpgm
	s_endpgm
	s_endpgm
	s_endpgm
	s_endpgm
	s_endpgm
	s_endpgm
	s_endpgm
	s_endpgm
	s_endpgm
	s_endpgm
	s_endpgm
	s_endpgm
	s_endpgm
	s_endpgm
	s_endpgm
	s_endpgm
	s_endpgm
	s_endpgm
	s_endpgm
	s_endpgm
	s_endpgm
	s_endpgm
	s_endpgm
	s_endpgm
	s_endpgm
	s_endpgm
	s_endpgm
	s_endpgm
	s_endpgm
	s_endpgm
	s_endpgm
	s_endpgm
	s_endpgm
	s_endpgm
	s_endpgm
	s_endpgm
	s_endpgm
	s_endpgm
	s_endpgm
	s_endpgm
	s_endpgm
	s_endpgm
	s_endpgm
	s_endpgm
	s_endpgm
	s_endpgm
	s_endpgm
	s_endpgm
	s_endpgm
	s_endpgm
	s_endpgm
	s_endpgm
	s_endpgm
